# s13
# speedup vs baseline: 1.0620x; 1.0073x over previous
.LBB1_14:
	s_or_b64 exec, exec, s[0:1]
	s_cmp_lg_u32 s2, 0x1800000
	s_cselect_b32 s32, 0x800000, 0
	s_add_u32 s100, s22, s32
	s_addc_u32 s101, s90, 0
	global_load_dwordx4 v[216:219], v201, s[100:101] nt
	s_add_u32 s100, s22, s32
	s_addc_u32 s101, s90, 0
	s_add_u32 s100, s100, 0x20000
	s_addc_u32 s101, s101, 0
	global_load_dwordx4 v[220:223], v201, s[100:101] nt
	s_add_u32 s100, s22, s32
	s_addc_u32 s101, s90, 0
	s_add_u32 s100, s100, 0x40000
	s_addc_u32 s101, s101, 0
	global_load_dwordx4 v[224:227], v201, s[100:101] nt
	s_add_u32 s100, s22, s32
	s_addc_u32 s101, s90, 0
	s_add_u32 s100, s100, 0x60000
	s_addc_u32 s101, s101, 0
	global_load_dwordx4 v[228:231], v201, s[100:101] nt
	s_add_u32 s100, s22, s32
	s_addc_u32 s101, s90, 0
	s_add_u32 s100, s100, 0x80000
	s_addc_u32 s101, s101, 0
	global_load_dwordx4 v[232:235], v201, s[100:101] nt
	s_add_u32 s100, s22, s32
	s_addc_u32 s101, s90, 0
	s_add_u32 s100, s100, 0xa0000
	s_addc_u32 s101, s101, 0
	global_load_dwordx4 v[236:239], v201, s[100:101] nt
	s_add_u32 s100, s22, s32
	s_addc_u32 s101, s90, 0
	s_add_u32 s100, s100, 0xc0000
	s_addc_u32 s101, s101, 0
	global_load_dwordx4 v[240:243], v201, s[100:101] nt
	s_add_u32 s100, s22, s32
	s_addc_u32 s101, s90, 0
	s_add_u32 s100, s100, 0xe0000
	s_addc_u32 s101, s101, 0
	global_load_dwordx4 v[244:247], v201, s[100:101] nt
	v_exp_f32_e32 v154, v154
	v_exp_f32_e32 v155, v155
	v_exp_f32_e32 v156, v156
	v_exp_f32_e32 v157, v157
	v_pk_add_f32 v[154:155], v[154:155], 1.0 op_sel_hi:[1,0]
	v_pk_add_f32 v[156:157], v[156:157], 1.0 op_sel_hi:[1,0]
	v_rcp_f32_e32 v154, v154
	v_rcp_f32_e32 v155, v155
	v_rcp_f32_e32 v156, v156
	v_rcp_f32_e32 v157, v157
	v_pk_mul_f32 v[248:249], v[154:155], v[90:91]
	v_pk_fma_f32 v[248:249], v[156:157], v[92:93], v[248:249]
	v_exp_f32_e32 v158, v158
	v_exp_f32_e32 v159, v159
	v_exp_f32_e32 v160, v160
	v_exp_f32_e32 v161, v161
	v_pk_add_f32 v[158:159], v[158:159], 1.0 op_sel_hi:[1,0]
	v_pk_add_f32 v[160:161], v[160:161], 1.0 op_sel_hi:[1,0]
	v_rcp_f32_e32 v158, v158
	v_rcp_f32_e32 v159, v159
	v_rcp_f32_e32 v160, v160
	v_rcp_f32_e32 v161, v161
	v_pk_fma_f32 v[248:249], v[158:159], v[102:103], v[248:249]
	v_pk_fma_f32 v[248:249], v[160:161], v[104:105], v[248:249]
	v_exp_f32_e32 v166, v166
	v_exp_f32_e32 v167, v167
	v_exp_f32_e32 v168, v168
	v_exp_f32_e32 v169, v169
	v_pk_add_f32 v[166:167], v[166:167], 1.0 op_sel_hi:[1,0]
	v_pk_add_f32 v[168:169], v[168:169], 1.0 op_sel_hi:[1,0]
	v_rcp_f32_e32 v166, v166
	v_rcp_f32_e32 v167, v167
	v_rcp_f32_e32 v168, v168
	v_rcp_f32_e32 v169, v169
	v_pk_fma_f32 v[248:249], v[166:167], v[86:87], v[248:249]
	v_pk_fma_f32 v[248:249], v[168:169], v[88:89], v[248:249]
	v_exp_f32_e32 v170, v170
	v_exp_f32_e32 v171, v171
	v_exp_f32_e32 v172, v172
	v_exp_f32_e32 v173, v173
	v_pk_add_f32 v[170:171], v[170:171], 1.0 op_sel_hi:[1,0]
	v_pk_add_f32 v[172:173], v[172:173], 1.0 op_sel_hi:[1,0]
	v_rcp_f32_e32 v170, v170
	v_rcp_f32_e32 v171, v171
	v_rcp_f32_e32 v172, v172
	v_rcp_f32_e32 v173, v173
	v_pk_fma_f32 v[248:249], v[170:171], v[98:99], v[248:249]
	v_pk_fma_f32 v[248:249], v[172:173], v[100:101], v[248:249]
	v_exp_f32_e32 v178, v178
	v_exp_f32_e32 v179, v179
	v_exp_f32_e32 v180, v180
	v_exp_f32_e32 v181, v181
	v_pk_add_f32 v[178:179], v[178:179], 1.0 op_sel_hi:[1,0]
	v_pk_add_f32 v[180:181], v[180:181], 1.0 op_sel_hi:[1,0]
	v_rcp_f32_e32 v178, v178
	v_rcp_f32_e32 v179, v179
	v_rcp_f32_e32 v180, v180
	v_rcp_f32_e32 v181, v181
	v_pk_fma_f32 v[248:249], v[178:179], v[118:119], v[248:249]
	v_pk_fma_f32 v[248:249], v[180:181], v[120:121], v[248:249]
	v_exp_f32_e32 v182, v182
	v_exp_f32_e32 v183, v183
	v_exp_f32_e32 v184, v184
	v_exp_f32_e32 v185, v185
	v_pk_add_f32 v[182:183], v[182:183], 1.0 op_sel_hi:[1,0]
	v_pk_add_f32 v[184:185], v[184:185], 1.0 op_sel_hi:[1,0]
	v_rcp_f32_e32 v182, v182
	v_rcp_f32_e32 v183, v183
	v_rcp_f32_e32 v184, v184
	v_rcp_f32_e32 v185, v185
	v_pk_fma_f32 v[248:249], v[182:183], v[110:111], v[248:249]
	v_pk_fma_f32 v[248:249], v[184:185], v[112:113], v[248:249]
	v_exp_f32_e32 v186, v186
	v_exp_f32_e32 v187, v187
	v_exp_f32_e32 v188, v188
	v_exp_f32_e32 v189, v189
	v_pk_add_f32 v[186:187], v[186:187], 1.0 op_sel_hi:[1,0]
	v_pk_add_f32 v[188:189], v[188:189], 1.0 op_sel_hi:[1,0]
	v_rcp_f32_e32 v186, v186
	v_rcp_f32_e32 v187, v187
	v_rcp_f32_e32 v188, v188
	v_rcp_f32_e32 v189, v189
	v_pk_fma_f32 v[248:249], v[186:187], v[126:127], v[248:249]
	v_pk_fma_f32 v[248:249], v[188:189], v[128:129], v[248:249]
	v_exp_f32_e32 v190, v190
	v_exp_f32_e32 v191, v191
	v_exp_f32_e32 v192, v192
	v_exp_f32_e32 v193, v193
	v_pk_add_f32 v[190:191], v[190:191], 1.0 op_sel_hi:[1,0]
	v_pk_add_f32 v[192:193], v[192:193], 1.0 op_sel_hi:[1,0]
	v_rcp_f32_e32 v190, v190
	v_rcp_f32_e32 v191, v191
	v_rcp_f32_e32 v192, v192
	v_rcp_f32_e32 v193, v193
	v_pk_fma_f32 v[248:249], v[190:191], v[122:123], v[248:249]
	v_pk_fma_f32 v[248:249], v[192:193], v[124:125], v[248:249]
	v_add_f32_e32 v158, v248, v249
	ds_bpermute_b32 v154, v206, v158
	s_waitcnt vmcnt(10)
	v_cmp_eq_u32_e64 s[0:1], 0, v211
	s_waitcnt lgkmcnt(0)
	v_add_f32_e32 v154, v158, v154
	ds_bpermute_b32 v155, v205, v154
	s_waitcnt lgkmcnt(0)
	v_add_f32_e32 v154, v154, v155
	v_add_f32_e32 v154, v212, v154
	v_mul_f32_e32 v154, 0x3fb8aa3b, v154
	v_exp_f32_e32 v154, v154
	s_nop 0
	v_cndmask_b32_e64 v154, 0, v154, s[0:1]
	s_and_saveexec_b64 s[0:1], vcc
	s_cbranch_execz .LBB1_16
	global_store_dword v[198:199], v154, off offset:64
.LBB1_16:
	s_or_b64 exec, exec, s[0:1]
	s_add_u32 s100, s22, s32
	s_addc_u32 s101, s90, 0
	s_add_u32 s100, s100, 0x100
	s_addc_u32 s101, s101, 0
	global_load_dwordx4 v[156:159], v201, s[100:101] nt
	s_add_u32 s100, s22, s32
	s_addc_u32 s101, s90, 0
	s_add_u32 s100, s100, 0x20100
	s_addc_u32 s101, s101, 0
	global_load_dwordx4 v[168:171], v201, s[100:101] nt
	s_add_u32 s100, s22, s32
	s_addc_u32 s101, s90, 0
	s_add_u32 s100, s100, 0x40100
	s_addc_u32 s101, s101, 0
	global_load_dwordx4 v[180:183], v201, s[100:101] nt
	s_add_u32 s100, s22, s32
	s_addc_u32 s101, s90, 0
	s_add_u32 s100, s100, 0x60100
	s_addc_u32 s101, s101, 0
	global_load_dwordx4 v[184:187], v201, s[100:101] nt
	s_add_u32 s100, s22, s32
	s_addc_u32 s101, s90, 0
	s_add_u32 s100, s100, 0x80100
	s_addc_u32 s101, s101, 0
	global_load_dwordx4 v[188:191], v201, s[100:101] nt
	v_exp_f32_e32 v106, v106
	v_exp_f32_e32 v107, v107
	v_exp_f32_e32 v108, v108
	v_exp_f32_e32 v109, v109
	v_pk_add_f32 v[106:107], v[106:107], 1.0 op_sel_hi:[1,0]
	v_pk_add_f32 v[108:109], v[108:109], 1.0 op_sel_hi:[1,0]
	v_rcp_f32_e32 v106, v106
	v_rcp_f32_e32 v107, v107
	v_rcp_f32_e32 v108, v108
	v_rcp_f32_e32 v109, v109
	v_pk_mul_f32 v[248:249], v[106:107], v[90:91]
	v_pk_fma_f32 v[248:249], v[108:109], v[92:93], v[248:249]
	v_exp_f32_e32 v114, v114
	v_exp_f32_e32 v115, v115
	v_exp_f32_e32 v116, v116
	v_exp_f32_e32 v117, v117
	v_pk_add_f32 v[114:115], v[114:115], 1.0 op_sel_hi:[1,0]
	v_pk_add_f32 v[116:117], v[116:117], 1.0 op_sel_hi:[1,0]
	v_rcp_f32_e32 v114, v114
	v_rcp_f32_e32 v115, v115
	v_rcp_f32_e32 v116, v116
	v_rcp_f32_e32 v117, v117
	v_pk_fma_f32 v[248:249], v[114:115], v[102:103], v[248:249]
	v_pk_fma_f32 v[248:249], v[116:117], v[104:105], v[248:249]
	v_exp_f32_e32 v134, v134
	v_exp_f32_e32 v135, v135
	v_exp_f32_e32 v136, v136
	v_exp_f32_e32 v137, v137
	v_pk_add_f32 v[134:135], v[134:135], 1.0 op_sel_hi:[1,0]
	v_pk_add_f32 v[136:137], v[136:137], 1.0 op_sel_hi:[1,0]
	v_rcp_f32_e32 v134, v134
	v_rcp_f32_e32 v135, v135
	v_rcp_f32_e32 v136, v136
	v_rcp_f32_e32 v137, v137
	v_pk_fma_f32 v[248:249], v[134:135], v[86:87], v[248:249]
	v_pk_fma_f32 v[248:249], v[136:137], v[88:89], v[248:249]
	v_exp_f32_e32 v138, v138
	v_exp_f32_e32 v139, v139
	v_exp_f32_e32 v140, v140
	v_exp_f32_e32 v141, v141
	v_pk_add_f32 v[138:139], v[138:139], 1.0 op_sel_hi:[1,0]
	v_pk_add_f32 v[140:141], v[140:141], 1.0 op_sel_hi:[1,0]
	v_rcp_f32_e32 v138, v138
	v_rcp_f32_e32 v139, v139
	v_rcp_f32_e32 v140, v140
	v_rcp_f32_e32 v141, v141
	v_pk_fma_f32 v[248:249], v[138:139], v[98:99], v[248:249]
	v_pk_fma_f32 v[248:249], v[140:141], v[100:101], v[248:249]
	v_exp_f32_e32 v146, v146
	v_exp_f32_e32 v147, v147
	v_exp_f32_e32 v148, v148
	v_exp_f32_e32 v149, v149
	v_pk_add_f32 v[146:147], v[146:147], 1.0 op_sel_hi:[1,0]
	v_pk_add_f32 v[148:149], v[148:149], 1.0 op_sel_hi:[1,0]
	v_rcp_f32_e32 v146, v146
	v_rcp_f32_e32 v147, v147
	v_rcp_f32_e32 v148, v148
	v_rcp_f32_e32 v149, v149
	v_pk_fma_f32 v[248:249], v[146:147], v[118:119], v[248:249]
	v_pk_fma_f32 v[248:249], v[148:149], v[120:121], v[248:249]
	v_exp_f32_e32 v150, v150
	v_exp_f32_e32 v151, v151
	v_exp_f32_e32 v152, v152
	v_exp_f32_e32 v153, v153
	v_pk_add_f32 v[150:151], v[150:151], 1.0 op_sel_hi:[1,0]
	v_pk_add_f32 v[152:153], v[152:153], 1.0 op_sel_hi:[1,0]
	v_rcp_f32_e32 v150, v150
	v_rcp_f32_e32 v151, v151
	v_rcp_f32_e32 v152, v152
	v_rcp_f32_e32 v153, v153
	v_pk_fma_f32 v[248:249], v[150:151], v[110:111], v[248:249]
	v_pk_fma_f32 v[248:249], v[152:153], v[112:113], v[248:249]
	v_exp_f32_e32 v162, v162
	v_exp_f32_e32 v163, v163
	v_exp_f32_e32 v164, v164
	v_exp_f32_e32 v165, v165
	v_pk_add_f32 v[162:163], v[162:163], 1.0 op_sel_hi:[1,0]
	v_pk_add_f32 v[164:165], v[164:165], 1.0 op_sel_hi:[1,0]
	v_rcp_f32_e32 v162, v162
	v_rcp_f32_e32 v163, v163
	v_rcp_f32_e32 v164, v164
	v_rcp_f32_e32 v165, v165
	v_pk_fma_f32 v[248:249], v[162:163], v[126:127], v[248:249]
	v_pk_fma_f32 v[248:249], v[164:165], v[128:129], v[248:249]
	v_exp_f32_e32 v174, v174
	v_exp_f32_e32 v175, v175
	v_exp_f32_e32 v176, v176
	v_exp_f32_e32 v177, v177
	v_pk_add_f32 v[174:175], v[174:175], 1.0 op_sel_hi:[1,0]
	v_pk_add_f32 v[176:177], v[176:177], 1.0 op_sel_hi:[1,0]
	v_rcp_f32_e32 v174, v174
	v_rcp_f32_e32 v175, v175
	v_rcp_f32_e32 v176, v176
	v_rcp_f32_e32 v177, v177
	v_pk_fma_f32 v[248:249], v[174:175], v[122:123], v[248:249]
	v_pk_fma_f32 v[248:249], v[176:177], v[124:125], v[248:249]
	v_add_f32_e32 v114, v248, v249
	ds_bpermute_b32 v106, v206, v114
	s_waitcnt vmcnt(14)
	v_cmp_eq_u32_e64 s[0:1], 0, v210
	s_waitcnt lgkmcnt(0)
	v_add_f32_e32 v106, v114, v106
	ds_bpermute_b32 v107, v205, v106
	s_waitcnt lgkmcnt(0)
	v_add_f32_e32 v106, v106, v107
	v_add_f32_e32 v106, v212, v106
	v_mul_f32_e32 v106, 0x3fb8aa3b, v106
	v_exp_f32_e32 v106, v106
	s_nop 0
	v_cndmask_b32_e64 v106, 0, v106, s[0:1]
	s_and_saveexec_b64 s[0:1], vcc
	s_cbranch_execz .LBB1_18
	global_store_dword v[198:199], v106, off offset:128
.LBB1_18:
	s_or_b64 exec, exec, s[0:1]
	s_add_u32 s100, s22, s32
	s_addc_u32 s101, s90, 0
	s_add_u32 s100, s100, 0xa0100
	s_addc_u32 s101, s101, 0
	global_load_dwordx4 v[136:139], v201, s[100:101] nt
	s_add_u32 s100, s22, s32
	s_addc_u32 s101, s90, 0
	s_add_u32 s100, s100, 0xc0100
	s_addc_u32 s101, s101, 0
	global_load_dwordx4 v[148:151], v201, s[100:101] nt
	s_add_u32 s100, s22, s32
	s_addc_u32 s101, s90, 0
	s_add_u32 s100, s100, 0xe0100
	s_addc_u32 s101, s101, 0
	global_load_dwordx4 v[160:163], v201, s[100:101] nt
	v_exp_f32_e32 v66, v66
	v_exp_f32_e32 v67, v67
	v_exp_f32_e32 v68, v68
	v_exp_f32_e32 v69, v69
	v_pk_add_f32 v[66:67], v[66:67], 1.0 op_sel_hi:[1,0]
	v_pk_add_f32 v[68:69], v[68:69], 1.0 op_sel_hi:[1,0]
	v_rcp_f32_e32 v66, v66
	v_rcp_f32_e32 v67, v67
	v_rcp_f32_e32 v68, v68
	v_rcp_f32_e32 v69, v69
	v_pk_mul_f32 v[248:249], v[66:67], v[102:103]
	v_pk_fma_f32 v[248:249], v[68:69], v[104:105], v[248:249]
	v_exp_f32_e32 v70, v70
	v_exp_f32_e32 v71, v71
	v_exp_f32_e32 v72, v72
	v_exp_f32_e32 v73, v73
	v_pk_add_f32 v[70:71], v[70:71], 1.0 op_sel_hi:[1,0]
	v_pk_add_f32 v[72:73], v[72:73], 1.0 op_sel_hi:[1,0]
	v_rcp_f32_e32 v70, v70
	v_rcp_f32_e32 v71, v71
	v_rcp_f32_e32 v72, v72
	v_rcp_f32_e32 v73, v73
	v_pk_fma_f32 v[248:249], v[70:71], v[90:91], v[248:249]
	v_pk_fma_f32 v[248:249], v[72:73], v[92:93], v[248:249]
	v_exp_f32_e32 v74, v74
	v_exp_f32_e32 v75, v75
	v_exp_f32_e32 v76, v76
	v_exp_f32_e32 v77, v77
	v_pk_add_f32 v[74:75], v[74:75], 1.0 op_sel_hi:[1,0]
	v_pk_add_f32 v[76:77], v[76:77], 1.0 op_sel_hi:[1,0]
	v_rcp_f32_e32 v74, v74
	v_rcp_f32_e32 v75, v75
	v_rcp_f32_e32 v76, v76
	v_rcp_f32_e32 v77, v77
	v_pk_fma_f32 v[248:249], v[74:75], v[98:99], v[248:249]
	v_pk_fma_f32 v[248:249], v[76:77], v[100:101], v[248:249]
	v_exp_f32_e32 v78, v78
	v_exp_f32_e32 v79, v79
	v_exp_f32_e32 v80, v80
	v_exp_f32_e32 v81, v81
	v_pk_add_f32 v[78:79], v[78:79], 1.0 op_sel_hi:[1,0]
	v_pk_add_f32 v[80:81], v[80:81], 1.0 op_sel_hi:[1,0]
	v_rcp_f32_e32 v78, v78
	v_rcp_f32_e32 v79, v79
	v_rcp_f32_e32 v80, v80
	v_rcp_f32_e32 v81, v81
	v_pk_fma_f32 v[248:249], v[78:79], v[86:87], v[248:249]
	v_pk_fma_f32 v[248:249], v[80:81], v[88:89], v[248:249]
	v_exp_f32_e32 v82, v82
	v_exp_f32_e32 v83, v83
	v_exp_f32_e32 v84, v84
	v_exp_f32_e32 v85, v85
	v_pk_add_f32 v[82:83], v[82:83], 1.0 op_sel_hi:[1,0]
	v_pk_add_f32 v[84:85], v[84:85], 1.0 op_sel_hi:[1,0]
	v_rcp_f32_e32 v82, v82
	v_rcp_f32_e32 v83, v83
	v_rcp_f32_e32 v84, v84
	v_rcp_f32_e32 v85, v85
	v_pk_fma_f32 v[248:249], v[82:83], v[118:119], v[248:249]
	v_pk_fma_f32 v[248:249], v[84:85], v[120:121], v[248:249]
	v_exp_f32_e32 v94, v94
	v_exp_f32_e32 v95, v95
	v_exp_f32_e32 v96, v96
	v_exp_f32_e32 v97, v97
	v_pk_add_f32 v[94:95], v[94:95], 1.0 op_sel_hi:[1,0]
	v_pk_add_f32 v[96:97], v[96:97], 1.0 op_sel_hi:[1,0]
	v_rcp_f32_e32 v94, v94
	v_rcp_f32_e32 v95, v95
	v_rcp_f32_e32 v96, v96
	v_rcp_f32_e32 v97, v97
	v_pk_fma_f32 v[248:249], v[94:95], v[110:111], v[248:249]
	v_pk_fma_f32 v[248:249], v[96:97], v[112:113], v[248:249]
	v_exp_f32_e32 v130, v130
	v_exp_f32_e32 v131, v131
	v_exp_f32_e32 v132, v132
	v_exp_f32_e32 v133, v133
	v_pk_add_f32 v[130:131], v[130:131], 1.0 op_sel_hi:[1,0]
	v_pk_add_f32 v[132:133], v[132:133], 1.0 op_sel_hi:[1,0]
	v_rcp_f32_e32 v130, v130
	v_rcp_f32_e32 v131, v131
	v_rcp_f32_e32 v132, v132
	v_rcp_f32_e32 v133, v133
	v_pk_fma_f32 v[248:249], v[130:131], v[126:127], v[248:249]
	v_pk_fma_f32 v[248:249], v[132:133], v[128:129], v[248:249]
	v_exp_f32_e32 v142, v142
	v_exp_f32_e32 v143, v143
	v_exp_f32_e32 v144, v144
	v_exp_f32_e32 v145, v145
	v_pk_add_f32 v[142:143], v[142:143], 1.0 op_sel_hi:[1,0]
	v_pk_add_f32 v[144:145], v[144:145], 1.0 op_sel_hi:[1,0]
	v_rcp_f32_e32 v142, v142
	v_rcp_f32_e32 v143, v143
	v_rcp_f32_e32 v144, v144
	v_rcp_f32_e32 v145, v145
	v_pk_fma_f32 v[248:249], v[142:143], v[122:123], v[248:249]
	v_pk_fma_f32 v[248:249], v[144:145], v[124:125], v[248:249]
	v_add_f32_e32 v66, v248, v249
	ds_bpermute_b32 v67, v206, v66
	s_waitcnt vmcnt(16)
	v_cmp_eq_u32_e64 s[0:1], 0, v209
	s_waitcnt lgkmcnt(0)
	v_add_f32_e32 v66, v66, v67
	ds_bpermute_b32 v67, v205, v66
	s_waitcnt lgkmcnt(0)
	v_add_f32_e32 v66, v66, v67
	v_add_f32_e32 v66, v212, v66
	v_mul_f32_e32 v66, 0x3fb8aa3b, v66
	v_exp_f32_e32 v66, v66
	s_nop 0
	v_cndmask_b32_e64 v66, 0, v66, s[0:1]
	s_and_saveexec_b64 s[0:1], vcc
	s_cbranch_execz .LBB1_20
	global_store_dword v[198:199], v66, off offset:192
